# wo: K-slabs via global_load_lds into a 4-stage LDS ring (3 slabs in flight, counted vmcnt), no register staging
# baseline (speedup 1.0000x reference)
.LBB2_2:
	s_lshl_b32 s0, s2, 2
	s_and_b32 s0, s0, 12
	s_bfe_u32 s1, s2, 0x20003
	s_or_b32 s0, s0, s1
	s_lshl_b32 s3, s0, 7
	s_lshl_b32 s0, s2, 1
	s_and_b32 s0, s0, 8
	s_lshr_b32 s1, s2, 5
	s_add_i32 s0, s0, s1
	s_lshl_b32 s2, s0, 7
	v_lshrrev_b32_e32 v32, 3, v0
	v_or_b32_e32 v2, s2, v32
	v_ashrrev_i32_e32 v3, 31, v2
	v_lshlrev_b64 v[2:3], 12, v[2:3]
	s_waitcnt lgkmcnt(0)
	v_lshl_add_u64 v[4:5], s[6:7], 0, v[2:3]
	v_lshlrev_b32_e32 v2, 4, v0
	v_or_b32_e32 v1, s3, v32
	v_and_b32_e32 v2, 0x70, v2
	v_mov_b32_e32 v3, 0
	v_lshl_add_u64 v[98:99], v[4:5], 0, v[2:3]
	v_lshlrev_b32_e32 v4, 12, v1
	v_mov_b32_e32 v5, v3
	v_lshl_add_u64 v[4:5], s[4:5], 0, v[4:5]
	v_lshl_add_u64 v[100:101], v[4:5], 0, v[2:3]
	v_lshrrev_b32_e32 v154, 4, v0
	v_xor_b32_e32 v154, v154, v0
	v_lshlrev_b32_e32 v154, 4, v154
	v_and_b32_e32 v154, 0x70, v154
	v_sub_u32_e32 v154, v154, v2
	v_ashrrev_i32_e32 v155, 31, v154
	v_lshl_add_u64 v[146:147], v[100:101], 0, v[154:155]
	v_lshl_add_u64 v[150:151], v[98:99], 0, v[154:155]
	s_mov_b64 s[12:13], 0x40000
	s_mov_b64 s[14:15], 0x80
	v_lshl_add_u64 v[148:149], v[146:147], 0, s[12:13]
	v_lshl_add_u64 v[152:153], v[150:151], 0, s[12:13]
	v_readfirstlane_b32 s10, v0
	s_lshl_b32 s10, s10, 4
	s_mov_b32 s4, 0x40000
	v_add_co_u32_e32 v28, vcc, s4, v100
	v_addc_co_u32_e32 v29, vcc, 0, v101, vcc
	v_add_co_u32_e32 v30, vcc, s4, v98
	s_nop 0
	v_addc_co_u32_e32 v31, vcc, 0, v99, vcc
	v_lshrrev_b32_e32 v2, 4, v0
	v_lshrrev_b32_e32 v104, 6, v0
	v_lshrrev_b32_e32 v105, 8, v0
	v_xor_b32_e32 v2, v2, v0
	v_bfe_u32 v103, v0, 5, 1
	v_lshlrev_b32_e32 v34, 2, v105
	v_lshlrev_b32_e32 v102, 5, v104
	v_lshlrev_b32_e32 v2, 4, v2
	v_and_b32_e32 v1, 31, v0
	v_bfe_u32 v33, v0, 1, 3
	v_lshlrev_b32_e32 v4, 7, v0
	v_or_b32_e32 v36, v34, v103
	v_and_b32_e32 v106, 64, v102
	v_and_b32_e32 v2, 0x70, v2
	v_and_b32_e32 v35, 0x2f80, v4
	v_bitop3_b32 v28, v34, v33, v103 bitop3:0x36
	v_bitop3_b32 v30, v36, v33, 2 bitop3:0x36
	v_or_b32_e32 v31, v106, v1
	v_lshl_or_b32 v2, v32, 7, v2
	v_add_u32_e32 v29, 0, v35
	v_lshlrev_b32_e32 v28, 4, v28
	v_lshl_add_u32 v31, v31, 7, 0
	v_lshlrev_b32_e32 v30, 4, v30
	v_add_u32_e32 v108, 0, v2
	s_mov_b32 s1, 0
	s_mov_b32 s5, -2
	v_mov_b32_e32 v4, v3
	v_mov_b32_e32 v5, v3
	v_mov_b32_e32 v6, v3
	v_mov_b32_e32 v7, v3
	v_mov_b32_e32 v8, v3
	v_mov_b32_e32 v9, v3
	v_mov_b32_e32 v10, v3
	v_mov_b32_e32 v11, v3
	v_add_u32_e32 v107, v29, v28
	v_add_u32_e32 v109, v31, v28
	v_add_u32_e32 v110, v31, v30
	v_add_u32_e32 v111, v29, v30
	v_mov_b32_e32 v2, v3
	v_mov_b32_e32 v28, v3
	v_mov_b32_e32 v29, v3
	v_mov_b32_e32 v30, v3
	v_mov_b32_e32 v31, v3
	v_mov_b32_e32 v32, v3
	v_mov_b32_e32 v33, v3
	v_mov_b32_e32 v34, v3
	v_mov_b32_e32 v35, v3
	v_mov_b32_e32 v36, v3
	v_mov_b32_e32 v37, v3
	v_mov_b32_e32 v38, v3
	v_mov_b32_e32 v39, v3
	v_mov_b32_e32 v40, v3
	v_mov_b32_e32 v41, v3
	v_mov_b32_e32 v42, v3
	v_mov_b32_e32 v43, v3
	v_mov_b32_e32 v44, v3
	v_mov_b32_e32 v45, v3
	v_mov_b32_e32 v46, v3
	v_mov_b32_e32 v47, v3
	v_mov_b32_e32 v12, v3
	v_mov_b32_e32 v13, v3
	v_mov_b32_e32 v14, v3
	v_mov_b32_e32 v15, v3
	v_mov_b32_e32 v16, v3
	v_mov_b32_e32 v17, v3
	v_mov_b32_e32 v18, v3
	v_mov_b32_e32 v19, v3
	v_mov_b32_e32 v20, v3
	v_mov_b32_e32 v21, v3
	v_mov_b32_e32 v22, v3
	v_mov_b32_e32 v23, v3
	v_mov_b32_e32 v24, v3
	v_mov_b32_e32 v25, v3
	v_mov_b32_e32 v26, v3
	v_mov_b32_e32 v27, v3
	v_mov_b32_e32 v48, v3
	v_mov_b32_e32 v49, v3
	v_mov_b32_e32 v50, v3
	v_mov_b32_e32 v51, v3
	v_mov_b32_e32 v52, v3
	v_mov_b32_e32 v53, v3
	v_mov_b32_e32 v54, v3
	v_mov_b32_e32 v55, v3
	v_mov_b32_e32 v56, v3
	v_mov_b32_e32 v57, v3
	v_mov_b32_e32 v58, v3
	v_mov_b32_e32 v59, v3
	v_mov_b32_e32 v60, v3
	v_mov_b32_e32 v61, v3
	v_mov_b32_e32 v62, v3
	v_mov_b32_e32 v63, v3
	v_mov_b32_e32 v64, v3
	v_mov_b32_e32 v65, v3
	v_and_b32_e32 v112, 63, v0
	v_add_u32_e32 v156, 0x10000, v109
	v_add_u32_e32 v157, 0x10000, v110
	v_add_u32_e32 v158, 0x10000, v107
	v_add_u32_e32 v159, 0x10000, v111
	s_add_u32 m0, s10, 0x0
	s_nop 0
	global_load_lds_dwordx4 v[146:147], off
	s_add_u32 m0, s10, 0x2000
	s_nop 0
	global_load_lds_dwordx4 v[148:149], off
	s_add_u32 m0, s10, 0x4000
	s_nop 0
	global_load_lds_dwordx4 v[150:151], off
	s_add_u32 m0, s10, 0x6000
	s_nop 0
	global_load_lds_dwordx4 v[152:153], off
	v_lshl_add_u64 v[146:147], v[146:147], 0, s[14:15]
	v_lshl_add_u64 v[148:149], v[148:149], 0, s[14:15]
	v_lshl_add_u64 v[150:151], v[150:151], 0, s[14:15]
	v_lshl_add_u64 v[152:153], v[152:153], 0, s[14:15]
	s_add_u32 m0, s10, 0x8000
	s_nop 0
	global_load_lds_dwordx4 v[146:147], off
	s_add_u32 m0, s10, 0xa000
	s_nop 0
	global_load_lds_dwordx4 v[148:149], off
	s_add_u32 m0, s10, 0xc000
	s_nop 0
	global_load_lds_dwordx4 v[150:151], off
	s_add_u32 m0, s10, 0xe000
	s_nop 0
	global_load_lds_dwordx4 v[152:153], off
	v_lshl_add_u64 v[146:147], v[146:147], 0, s[14:15]
	v_lshl_add_u64 v[148:149], v[148:149], 0, s[14:15]
	v_lshl_add_u64 v[150:151], v[150:151], 0, s[14:15]
	v_lshl_add_u64 v[152:153], v[152:153], 0, s[14:15]
	s_add_u32 m0, s10, 0x10000
	s_nop 0
	global_load_lds_dwordx4 v[146:147], off
	s_add_u32 m0, s10, 0x12000
	s_nop 0
	global_load_lds_dwordx4 v[148:149], off
	s_add_u32 m0, s10, 0x14000
	s_nop 0
	global_load_lds_dwordx4 v[150:151], off
	s_add_u32 m0, s10, 0x16000
	s_nop 0
	global_load_lds_dwordx4 v[152:153], off
	v_lshl_add_u64 v[146:147], v[146:147], 0, s[14:15]
	v_lshl_add_u64 v[148:149], v[148:149], 0, s[14:15]
	v_lshl_add_u64 v[150:151], v[150:151], 0, s[14:15]
	v_lshl_add_u64 v[152:153], v[152:153], 0, s[14:15]
	s_waitcnt vmcnt(8)
	s_waitcnt lgkmcnt(0)
	s_barrier
	s_mov_b32 s5, 0
.Lwo_loop:
	s_add_u32 m0, s10, 0x18000
	s_nop 0
	global_load_lds_dwordx4 v[146:147], off
	s_add_u32 m0, s10, 0x1a000
	s_nop 0
	global_load_lds_dwordx4 v[148:149], off
	s_add_u32 m0, s10, 0x1c000
	s_nop 0
	global_load_lds_dwordx4 v[150:151], off
	s_add_u32 m0, s10, 0x1e000
	s_nop 0
	global_load_lds_dwordx4 v[152:153], off
	v_lshl_add_u64 v[146:147], v[146:147], 0, s[14:15]
	v_lshl_add_u64 v[148:149], v[148:149], 0, s[14:15]
	v_lshl_add_u64 v[150:151], v[150:151], 0, s[14:15]
	v_lshl_add_u64 v[152:153], v[152:153], 0, s[14:15]
	ds_read_b128 v[114:117], v109
	ds_read_b128 v[122:125], v107 offset:16384
	ds_read_b128 v[126:129], v107 offset:20480
	ds_read_b128 v[118:121], v109 offset:4096
	ds_read_b128 v[130:133], v110
	ds_read_b128 v[134:137], v111 offset:16384
	ds_read_b128 v[138:141], v111 offset:20480
	ds_read_b128 v[142:145], v110 offset:4096
	s_waitcnt lgkmcnt(6)
	v_mfma_f32_32x32x16_f16 v[50:65], v[114:117], v[122:125], v[50:65]
	s_waitcnt lgkmcnt(5)
	v_mfma_f32_32x32x16_f16 v[34:49], v[114:117], v[126:129], v[34:49]
	s_waitcnt lgkmcnt(4)
	v_mfma_f32_32x32x16_f16 v[18:33], v[118:121], v[122:125], v[18:33]
	v_mfma_f32_32x32x16_f16 v[2:17], v[118:121], v[126:129], v[2:17]
	s_waitcnt lgkmcnt(2)
	v_mfma_f32_32x32x16_f16 v[50:65], v[130:133], v[134:137], v[50:65]
	s_waitcnt lgkmcnt(1)
	v_mfma_f32_32x32x16_f16 v[34:49], v[130:133], v[138:141], v[34:49]
	s_waitcnt lgkmcnt(0)
	v_mfma_f32_32x32x16_f16 v[18:33], v[142:145], v[134:137], v[18:33]
	v_mfma_f32_32x32x16_f16 v[2:17], v[142:145], v[138:141], v[2:17]
	s_waitcnt vmcnt(8)
	s_barrier
	s_add_u32 m0, s10, 0x0
	s_nop 0
	global_load_lds_dwordx4 v[146:147], off
	s_add_u32 m0, s10, 0x2000
	s_nop 0
	global_load_lds_dwordx4 v[148:149], off
	s_add_u32 m0, s10, 0x4000
	s_nop 0
	global_load_lds_dwordx4 v[150:151], off
	s_add_u32 m0, s10, 0x6000
	s_nop 0
	global_load_lds_dwordx4 v[152:153], off
	v_lshl_add_u64 v[146:147], v[146:147], 0, s[14:15]
	v_lshl_add_u64 v[148:149], v[148:149], 0, s[14:15]
	v_lshl_add_u64 v[150:151], v[150:151], 0, s[14:15]
	v_lshl_add_u64 v[152:153], v[152:153], 0, s[14:15]
	ds_read_b128 v[114:117], v109 offset:32768
	ds_read_b128 v[122:125], v107 offset:49152
	ds_read_b128 v[126:129], v107 offset:53248
	ds_read_b128 v[118:121], v109 offset:36864
	ds_read_b128 v[130:133], v110 offset:32768
	ds_read_b128 v[134:137], v111 offset:49152
	ds_read_b128 v[138:141], v111 offset:53248
	ds_read_b128 v[142:145], v110 offset:36864
	s_waitcnt lgkmcnt(6)
	v_mfma_f32_32x32x16_f16 v[50:65], v[114:117], v[122:125], v[50:65]
	s_waitcnt lgkmcnt(5)
	v_mfma_f32_32x32x16_f16 v[34:49], v[114:117], v[126:129], v[34:49]
	s_waitcnt lgkmcnt(4)
	v_mfma_f32_32x32x16_f16 v[18:33], v[118:121], v[122:125], v[18:33]
	v_mfma_f32_32x32x16_f16 v[2:17], v[118:121], v[126:129], v[2:17]
	s_waitcnt lgkmcnt(2)
	v_mfma_f32_32x32x16_f16 v[50:65], v[130:133], v[134:137], v[50:65]
	s_waitcnt lgkmcnt(1)
	v_mfma_f32_32x32x16_f16 v[34:49], v[130:133], v[138:141], v[34:49]
	s_waitcnt lgkmcnt(0)
	v_mfma_f32_32x32x16_f16 v[18:33], v[142:145], v[134:137], v[18:33]
	v_mfma_f32_32x32x16_f16 v[2:17], v[142:145], v[138:141], v[2:17]
	s_waitcnt vmcnt(8)
	s_barrier
	s_add_u32 m0, s10, 0x8000
	s_nop 0
	global_load_lds_dwordx4 v[146:147], off
	s_add_u32 m0, s10, 0xa000
	s_nop 0
	global_load_lds_dwordx4 v[148:149], off
	s_add_u32 m0, s10, 0xc000
	s_nop 0
	global_load_lds_dwordx4 v[150:151], off
	s_add_u32 m0, s10, 0xe000
	s_nop 0
	global_load_lds_dwordx4 v[152:153], off
	v_lshl_add_u64 v[146:147], v[146:147], 0, s[14:15]
	v_lshl_add_u64 v[148:149], v[148:149], 0, s[14:15]
	v_lshl_add_u64 v[150:151], v[150:151], 0, s[14:15]
	v_lshl_add_u64 v[152:153], v[152:153], 0, s[14:15]
	ds_read_b128 v[114:117], v156
	ds_read_b128 v[122:125], v158 offset:16384
	ds_read_b128 v[126:129], v158 offset:20480
	ds_read_b128 v[118:121], v156 offset:4096
	ds_read_b128 v[130:133], v157
	ds_read_b128 v[134:137], v159 offset:16384
	ds_read_b128 v[138:141], v159 offset:20480
	ds_read_b128 v[142:145], v157 offset:4096
	s_waitcnt lgkmcnt(6)
	v_mfma_f32_32x32x16_f16 v[50:65], v[114:117], v[122:125], v[50:65]
	s_waitcnt lgkmcnt(5)
	v_mfma_f32_32x32x16_f16 v[34:49], v[114:117], v[126:129], v[34:49]
	s_waitcnt lgkmcnt(4)
	v_mfma_f32_32x32x16_f16 v[18:33], v[118:121], v[122:125], v[18:33]
	v_mfma_f32_32x32x16_f16 v[2:17], v[118:121], v[126:129], v[2:17]
	s_waitcnt lgkmcnt(2)
	v_mfma_f32_32x32x16_f16 v[50:65], v[130:133], v[134:137], v[50:65]
	s_waitcnt lgkmcnt(1)
	v_mfma_f32_32x32x16_f16 v[34:49], v[130:133], v[138:141], v[34:49]
	s_waitcnt lgkmcnt(0)
	v_mfma_f32_32x32x16_f16 v[18:33], v[142:145], v[134:137], v[18:33]
	v_mfma_f32_32x32x16_f16 v[2:17], v[142:145], v[138:141], v[2:17]
	s_waitcnt vmcnt(8)
	s_barrier
	s_add_u32 m0, s10, 0x10000
	s_nop 0
	global_load_lds_dwordx4 v[146:147], off
	s_add_u32 m0, s10, 0x12000
	s_nop 0
	global_load_lds_dwordx4 v[148:149], off
	s_add_u32 m0, s10, 0x14000
	s_nop 0
	global_load_lds_dwordx4 v[150:151], off
	s_add_u32 m0, s10, 0x16000
	s_nop 0
	global_load_lds_dwordx4 v[152:153], off
	v_lshl_add_u64 v[146:147], v[146:147], 0, s[14:15]
	v_lshl_add_u64 v[148:149], v[148:149], 0, s[14:15]
	v_lshl_add_u64 v[150:151], v[150:151], 0, s[14:15]
	v_lshl_add_u64 v[152:153], v[152:153], 0, s[14:15]
	ds_read_b128 v[114:117], v156 offset:32768
	ds_read_b128 v[122:125], v158 offset:49152
	ds_read_b128 v[126:129], v158 offset:53248
	ds_read_b128 v[118:121], v156 offset:36864
	ds_read_b128 v[130:133], v157 offset:32768
	ds_read_b128 v[134:137], v159 offset:49152
	ds_read_b128 v[138:141], v159 offset:53248
	ds_read_b128 v[142:145], v157 offset:36864
	s_waitcnt lgkmcnt(6)
	v_mfma_f32_32x32x16_f16 v[50:65], v[114:117], v[122:125], v[50:65]
	s_waitcnt lgkmcnt(5)
	v_mfma_f32_32x32x16_f16 v[34:49], v[114:117], v[126:129], v[34:49]
	s_waitcnt lgkmcnt(4)
	v_mfma_f32_32x32x16_f16 v[18:33], v[118:121], v[122:125], v[18:33]
	v_mfma_f32_32x32x16_f16 v[2:17], v[118:121], v[126:129], v[2:17]
	s_waitcnt lgkmcnt(2)
	v_mfma_f32_32x32x16_f16 v[50:65], v[130:133], v[134:137], v[50:65]
	s_waitcnt lgkmcnt(1)
	v_mfma_f32_32x32x16_f16 v[34:49], v[130:133], v[138:141], v[34:49]
	s_waitcnt lgkmcnt(0)
	v_mfma_f32_32x32x16_f16 v[18:33], v[142:145], v[134:137], v[18:33]
	v_mfma_f32_32x32x16_f16 v[2:17], v[142:145], v[138:141], v[2:17]
	s_waitcnt vmcnt(8)
	s_barrier
	s_add_i32 s5, s5, 1
	s_cmp_lt_u32 s5, 7
	s_cbranch_scc1 .Lwo_loop
	s_add_u32 m0, s10, 0x18000
	s_nop 0
	global_load_lds_dwordx4 v[146:147], off
	s_add_u32 m0, s10, 0x1a000
	s_nop 0
	global_load_lds_dwordx4 v[148:149], off
	s_add_u32 m0, s10, 0x1c000
	s_nop 0
	global_load_lds_dwordx4 v[150:151], off
	s_add_u32 m0, s10, 0x1e000
	s_nop 0
	global_load_lds_dwordx4 v[152:153], off
	v_lshl_add_u64 v[146:147], v[146:147], 0, s[14:15]
	v_lshl_add_u64 v[148:149], v[148:149], 0, s[14:15]
	v_lshl_add_u64 v[150:151], v[150:151], 0, s[14:15]
	v_lshl_add_u64 v[152:153], v[152:153], 0, s[14:15]
	ds_read_b128 v[114:117], v109
	ds_read_b128 v[122:125], v107 offset:16384
	ds_read_b128 v[126:129], v107 offset:20480
	ds_read_b128 v[118:121], v109 offset:4096
	ds_read_b128 v[130:133], v110
	ds_read_b128 v[134:137], v111 offset:16384
	ds_read_b128 v[138:141], v111 offset:20480
	ds_read_b128 v[142:145], v110 offset:4096
	s_waitcnt lgkmcnt(6)
	v_mfma_f32_32x32x16_f16 v[50:65], v[114:117], v[122:125], v[50:65]
	s_waitcnt lgkmcnt(5)
	v_mfma_f32_32x32x16_f16 v[34:49], v[114:117], v[126:129], v[34:49]
	s_waitcnt lgkmcnt(4)
	v_mfma_f32_32x32x16_f16 v[18:33], v[118:121], v[122:125], v[18:33]
	v_mfma_f32_32x32x16_f16 v[2:17], v[118:121], v[126:129], v[2:17]
	s_waitcnt lgkmcnt(2)
	v_mfma_f32_32x32x16_f16 v[50:65], v[130:133], v[134:137], v[50:65]
	s_waitcnt lgkmcnt(1)
	v_mfma_f32_32x32x16_f16 v[34:49], v[130:133], v[138:141], v[34:49]
	s_waitcnt lgkmcnt(0)
	v_mfma_f32_32x32x16_f16 v[18:33], v[142:145], v[134:137], v[18:33]
	v_mfma_f32_32x32x16_f16 v[2:17], v[142:145], v[138:141], v[2:17]
	s_waitcnt vmcnt(8)
	s_barrier
	ds_read_b128 v[114:117], v109 offset:32768
	ds_read_b128 v[122:125], v107 offset:49152
	ds_read_b128 v[126:129], v107 offset:53248
	ds_read_b128 v[118:121], v109 offset:36864
	ds_read_b128 v[130:133], v110 offset:32768
	ds_read_b128 v[134:137], v111 offset:49152
	ds_read_b128 v[138:141], v111 offset:53248
	ds_read_b128 v[142:145], v110 offset:36864
	s_waitcnt lgkmcnt(6)
	v_mfma_f32_32x32x16_f16 v[50:65], v[114:117], v[122:125], v[50:65]
	s_waitcnt lgkmcnt(5)
	v_mfma_f32_32x32x16_f16 v[34:49], v[114:117], v[126:129], v[34:49]
	s_waitcnt lgkmcnt(4)
	v_mfma_f32_32x32x16_f16 v[18:33], v[118:121], v[122:125], v[18:33]
	v_mfma_f32_32x32x16_f16 v[2:17], v[118:121], v[126:129], v[2:17]
	s_waitcnt lgkmcnt(2)
	v_mfma_f32_32x32x16_f16 v[50:65], v[130:133], v[134:137], v[50:65]
	s_waitcnt lgkmcnt(1)
	v_mfma_f32_32x32x16_f16 v[34:49], v[130:133], v[138:141], v[34:49]
	s_waitcnt lgkmcnt(0)
	v_mfma_f32_32x32x16_f16 v[18:33], v[142:145], v[134:137], v[18:33]
	v_mfma_f32_32x32x16_f16 v[2:17], v[142:145], v[138:141], v[2:17]
	s_waitcnt vmcnt(4)
	s_barrier
	ds_read_b128 v[114:117], v156
	ds_read_b128 v[122:125], v158 offset:16384
	ds_read_b128 v[126:129], v158 offset:20480
	ds_read_b128 v[118:121], v156 offset:4096
	ds_read_b128 v[130:133], v157
	ds_read_b128 v[134:137], v159 offset:16384
	ds_read_b128 v[138:141], v159 offset:20480
	ds_read_b128 v[142:145], v157 offset:4096
	s_waitcnt lgkmcnt(6)
	v_mfma_f32_32x32x16_f16 v[50:65], v[114:117], v[122:125], v[50:65]
	s_waitcnt lgkmcnt(5)
	v_mfma_f32_32x32x16_f16 v[34:49], v[114:117], v[126:129], v[34:49]
	s_waitcnt lgkmcnt(4)
	v_mfma_f32_32x32x16_f16 v[18:33], v[118:121], v[122:125], v[18:33]
	v_mfma_f32_32x32x16_f16 v[2:17], v[118:121], v[126:129], v[2:17]
	s_waitcnt lgkmcnt(2)
	v_mfma_f32_32x32x16_f16 v[50:65], v[130:133], v[134:137], v[50:65]
	s_waitcnt lgkmcnt(1)
	v_mfma_f32_32x32x16_f16 v[34:49], v[130:133], v[138:141], v[34:49]
	s_waitcnt lgkmcnt(0)
	v_mfma_f32_32x32x16_f16 v[18:33], v[142:145], v[134:137], v[18:33]
	v_mfma_f32_32x32x16_f16 v[2:17], v[142:145], v[138:141], v[2:17]
	s_waitcnt vmcnt(0)
	s_barrier
	ds_read_b128 v[114:117], v156 offset:32768
	ds_read_b128 v[122:125], v158 offset:49152
	ds_read_b128 v[126:129], v158 offset:53248
	ds_read_b128 v[118:121], v156 offset:36864
	ds_read_b128 v[130:133], v157 offset:32768
	ds_read_b128 v[134:137], v159 offset:49152
	ds_read_b128 v[138:141], v159 offset:53248
	ds_read_b128 v[142:145], v157 offset:36864
	s_waitcnt lgkmcnt(6)
	v_mfma_f32_32x32x16_f16 v[50:65], v[114:117], v[122:125], v[50:65]
	s_waitcnt lgkmcnt(5)
	v_mfma_f32_32x32x16_f16 v[34:49], v[114:117], v[126:129], v[34:49]
	s_waitcnt lgkmcnt(4)
	v_mfma_f32_32x32x16_f16 v[18:33], v[118:121], v[122:125], v[18:33]
	v_mfma_f32_32x32x16_f16 v[2:17], v[118:121], v[126:129], v[2:17]
	s_waitcnt lgkmcnt(2)
	v_mfma_f32_32x32x16_f16 v[50:65], v[130:133], v[134:137], v[50:65]
	s_waitcnt lgkmcnt(1)
	v_mfma_f32_32x32x16_f16 v[34:49], v[130:133], v[138:141], v[34:49]
	s_waitcnt lgkmcnt(0)
	v_mfma_f32_32x32x16_f16 v[18:33], v[142:145], v[134:137], v[18:33]
	v_mfma_f32_32x32x16_f16 v[2:17], v[142:145], v[138:141], v[2:17]
	s_barrier
	s_nop 7
	s_nop 7
	v_cmp_ne_u32_e32 vcc, 0, v105
	s_waitcnt vmcnt(7)
	v_lshlrev_b32_e32 v66, 2, v112
	v_lshlrev_b32_e32 v67, 14, v104
	s_and_saveexec_b64 s[0:1], vcc
	s_cbranch_execz .LBB2_6
	v_and_b32_e32 v68, 0xc000, v67
	v_add3_u32 v68, 0, v66, v68
	ds_write2st64_b32 v68, v50, v51 offset1:1
	ds_write2st64_b32 v68, v52, v53 offset0:2 offset1:3
	ds_write2st64_b32 v68, v54, v55 offset0:4 offset1:5
	ds_write2st64_b32 v68, v56, v57 offset0:6 offset1:7
	ds_write2st64_b32 v68, v58, v59 offset0:8 offset1:9
	ds_write2st64_b32 v68, v60, v61 offset0:10 offset1:11
	ds_write2st64_b32 v68, v62, v63 offset0:12 offset1:13
	ds_write2st64_b32 v68, v64, v65 offset0:14 offset1:15
	ds_write2st64_b32 v68, v34, v35 offset0:16 offset1:17
	ds_write2st64_b32 v68, v36, v37 offset0:18 offset1:19
	ds_write2st64_b32 v68, v38, v39 offset0:20 offset1:21
	ds_write2st64_b32 v68, v40, v41 offset0:22 offset1:23
	ds_write2st64_b32 v68, v42, v43 offset0:24 offset1:25
	ds_write2st64_b32 v68, v44, v45 offset0:26 offset1:27
	ds_write2st64_b32 v68, v46, v47 offset0:28 offset1:29
	ds_write2st64_b32 v68, v48, v49 offset0:30 offset1:31
	ds_write2st64_b32 v68, v18, v19 offset0:32 offset1:33
	ds_write2st64_b32 v68, v20, v21 offset0:34 offset1:35
	ds_write2st64_b32 v68, v22, v23 offset0:36 offset1:37
	ds_write2st64_b32 v68, v24, v25 offset0:38 offset1:39
	ds_write2st64_b32 v68, v26, v27 offset0:40 offset1:41
	ds_write2st64_b32 v68, v28, v29 offset0:42 offset1:43
	ds_write2st64_b32 v68, v30, v31 offset0:44 offset1:45
	ds_write2st64_b32 v68, v32, v33 offset0:46 offset1:47
	ds_write2st64_b32 v68, v2, v3 offset0:48 offset1:49
	ds_write2st64_b32 v68, v4, v5 offset0:50 offset1:51
	ds_write2st64_b32 v68, v6, v7 offset0:52 offset1:53
	ds_write2st64_b32 v68, v8, v9 offset0:54 offset1:55
	ds_write2st64_b32 v68, v10, v11 offset0:56 offset1:57
	ds_write2st64_b32 v68, v12, v13 offset0:58 offset1:59
	ds_write2st64_b32 v68, v14, v15 offset0:60 offset1:61
	ds_write2st64_b32 v68, v16, v17 offset0:62 offset1:63

	.amdhsa_kernel _Z9wo_kernelPKDF16_S0_Pf
		.amdhsa_group_segment_fixed_size 65536
		.amdhsa_private_segment_fixed_size 0
		.amdhsa_kernarg_size 24
		.amdhsa_user_sgpr_count 2
		.amdhsa_user_sgpr_dispatch_ptr 0
		.amdhsa_user_sgpr_queue_ptr 0
		.amdhsa_user_sgpr_kernarg_segment_ptr 1
		.amdhsa_user_sgpr_dispatch_id 0
		.amdhsa_user_sgpr_kernarg_preload_length 0
		.amdhsa_user_sgpr_kernarg_preload_offset 0
		.amdhsa_user_sgpr_private_segment_size 0
		.amdhsa_uses_dynamic_stack 0
		.amdhsa_enable_private_segment 0
		.amdhsa_system_sgpr_workgroup_id_x 1
		.amdhsa_system_sgpr_workgroup_id_y 0
		.amdhsa_system_sgpr_workgroup_id_z 0
		.amdhsa_system_sgpr_workgroup_info 0
		.amdhsa_system_vgpr_workitem_id 0
		.amdhsa_next_free_vgpr 160
		.amdhsa_next_free_sgpr 16
		.amdhsa_accum_offset 160
		.amdhsa_reserve_vcc 1
		.amdhsa_float_round_mode_32 0
		.amdhsa_float_round_mode_16_64 0
		.amdhsa_float_denorm_mode_32 3
		.amdhsa_float_denorm_mode_16_64 3
		.amdhsa_dx10_clamp 1
		.amdhsa_ieee_mode 1
		.amdhsa_fp16_overflow 0
		.amdhsa_tg_split 0
		.amdhsa_exception_fp_ieee_invalid_op 0
		.amdhsa_exception_fp_denorm_src 0
		.amdhsa_exception_fp_ieee_div_zero 0
		.amdhsa_exception_fp_ieee_overflow 0
		.amdhsa_exception_fp_ieee_underflow 0
		.amdhsa_exception_fp_ieee_inexact 0
		.amdhsa_exception_int_div_zero 0
	.end_amdhsa_kernel

amdhsa.kernels:
  - .agpr_count:     0
    .args:
      - .actual_access:  read_only
        .address_space:  global
        .offset:         0
        .size:           8
        .value_kind:     global_buffer
      - .actual_access:  write_only
        .address_space:  global
        .offset:         8
        .size:           8
        .value_kind:     global_buffer
    .group_segment_fixed_size: 0
    .kernarg_segment_align: 8
    .kernarg_segment_size: 16
    .language:       OpenCL C
    .language_version:
      - 2
      - 0
    .max_flat_workgroup_size: 256
    .name:           _Z13conv_x_kernelPKfPDF16_
    .private_segment_fixed_size: 0
    .sgpr_count:     14
    .sgpr_spill_count: 0
    .symbol:         _Z13conv_x_kernelPKfPDF16_.kd
    .uniform_work_group_size: 1
    .uses_dynamic_stack: false
    .vgpr_count:     12
    .vgpr_spill_count: 0
    .wavefront_size: 64
  - .agpr_count:     0
    .args:
      - .actual_access:  read_only
        .address_space:  global
        .offset:         0
        .size:           8
        .value_kind:     global_buffer
      - .actual_access:  read_only
        .address_space:  global
        .offset:         8
        .size:           8
        .value_kind:     global_buffer
      - .actual_access:  read_only
        .address_space:  global
        .offset:         16
        .size:           8
        .value_kind:     global_buffer
      - .actual_access:  read_only
        .address_space:  global
        .offset:         24
        .size:           8
        .value_kind:     global_buffer
      - .actual_access:  write_only
        .address_space:  global
        .offset:         32
        .size:           8
        .value_kind:     global_buffer
      - .actual_access:  write_only
        .address_space:  global
        .offset:         40
        .size:           8
        .value_kind:     global_buffer
      - .actual_access:  read_only
        .address_space:  global
        .offset:         48
        .size:           8
        .value_kind:     global_buffer
      - .actual_access:  write_only
        .address_space:  global
        .offset:         56
        .size:           8
        .value_kind:     global_buffer
    .group_segment_fixed_size: 16640
    .kernarg_segment_align: 8
    .kernarg_segment_size: 64
    .language:       OpenCL C
    .language_version:
      - 2
      - 0
    .max_flat_workgroup_size: 256
    .name:           _Z13conv_w_kernelPKfS0_S0_S0_PDF16_S1_S0_S1_
    .private_segment_fixed_size: 0
    .sgpr_count:     26
    .sgpr_spill_count: 0
    .symbol:         _Z13conv_w_kernelPKfS0_S0_S0_PDF16_S1_S0_S1_.kd
    .uniform_work_group_size: 1
    .uses_dynamic_stack: false
    .vgpr_count:     31
    .vgpr_spill_count: 0
    .wavefront_size: 64
  - .agpr_count:     0
    .args:
      - .actual_access:  read_only
        .address_space:  global
        .offset:         0
        .size:           8
        .value_kind:     global_buffer
      - .actual_access:  read_only
        .address_space:  global
        .offset:         8
        .size:           8
        .value_kind:     global_buffer
      - .actual_access:  write_only
        .address_space:  global
        .offset:         16
        .size:           8
        .value_kind:     global_buffer
    .group_segment_fixed_size: 65536
    .kernarg_segment_align: 8
    .kernarg_segment_size: 24
    .language:       OpenCL C
    .language_version:
      - 2
      - 0
    .max_flat_workgroup_size: 512
    .name:           _Z9wo_kernelPKDF16_S0_Pf
    .private_segment_fixed_size: 0
    .sgpr_count:     22
    .sgpr_spill_count: 0
    .symbol:         _Z9wo_kernelPKDF16_S0_Pf.kd
    .uniform_work_group_size: 1
    .uses_dynamic_stack: false
    .vgpr_count:     160
    .vgpr_spill_count: 0
    .wavefront_size: 64
  - .agpr_count:     0
    .args:
      - .address_space:  global
        .offset:         0
        .size:           8
        .value_kind:     global_buffer
      - .address_space:  global
        .offset:         8
        .size:           8
        .value_kind:     global_buffer
      - .actual_access:  write_only
        .address_space:  global
        .offset:         16
        .size:           8
        .value_kind:     global_buffer
      - .actual_access:  write_only
        .address_space:  global
        .offset:         24
        .size:           8
        .value_kind:     global_buffer
    .group_segment_fixed_size: 0
    .kernarg_segment_align: 8
    .kernarg_segment_size: 32
    .language:       OpenCL C
    .language_version:
      - 2
      - 0
    .max_flat_workgroup_size: 512
    .name:           _Z10qkv_kernelPKDF16_S0_PDF16_S1_
    .private_segment_fixed_size: 0
    .sgpr_count:     44
    .sgpr_spill_count: 0
    .symbol:         _Z10qkv_kernelPKDF16_S0_PDF16_S1_.kd
    .uniform_work_group_size: 1
    .uses_dynamic_stack: false
    .vgpr_count:     200
    .vgpr_spill_count: 0
    .wavefront_size: 64
  - .agpr_count:     0
    .args:
      - .actual_access:  read_only
        .address_space:  global
        .offset:         0
        .size:           8
        .value_kind:     global_buffer
      - .actual_access:  read_only
        .address_space:  global
        .offset:         8
        .size:           8
        .value_kind:     global_buffer
      - .actual_access:  read_only
        .address_space:  global
        .offset:         16
        .size:           8
        .value_kind:     global_buffer
      - .actual_access:  read_only
        .address_space:  global
        .offset:         24
        .size:           8
        .value_kind:     global_buffer
      - .actual_access:  read_only
        .address_space:  global
        .offset:         32
        .size:           8
        .value_kind:     global_buffer
      - .actual_access:  read_only
        .address_space:  global
        .offset:         40
        .size:           8
        .value_kind:     global_buffer
      - .actual_access:  read_only
        .address_space:  global
        .offset:         48
        .size:           8
        .value_kind:     global_buffer
      - .actual_access:  write_only
        .address_space:  global
        .offset:         56
        .size:           8
        .value_kind:     global_buffer
      - .actual_access:  write_only
        .address_space:  global
        .offset:         64
        .size:           8
        .value_kind:     global_buffer
      - .actual_access:  write_only
        .address_space:  global
        .offset:         72
        .size:           8
        .value_kind:     global_buffer
    .group_segment_fixed_size: 0
    .kernarg_segment_align: 8
    .kernarg_segment_size: 80
    .language:       OpenCL C
    .language_version:
      - 2
      - 0
    .max_flat_workgroup_size: 512
    .name:           _Z11attn_kernelPKDF16_S0_PKfS2_S2_S2_S2_PfPDF16_S3_
    .private_segment_fixed_size: 0
    .sgpr_count:     44
    .sgpr_spill_count: 0
    .symbol:         _Z11attn_kernelPKDF16_S0_PKfS2_S2_S2_S2_PfPDF16_S3_.kd
    .uniform_work_group_size: 1
    .uses_dynamic_stack: false
    .vgpr_count:     256
    .vgpr_spill_count: 0
    .wavefront_size: 64
